# v55 + RG-LRU phases: stagger of the backward wave half doubled (s_sleep 16 instead of 8)
# speedup vs baseline: 1.0049x; 1.0049x over previous
; #define LAS __attribute__((address_space(3)))
; __device__ __forceinline__ int crow(int r, int hh) { return (r & 3) + 8 * (r >> 2) + 4 * hh; }
; template <bool FINAL, int z> __device__ __forceinline__ void rglru_blocks(LAS unsigned char* XCB, LAS float* XCF, LAS float* HS, const bf16x8 (&wa)[8], const bf16x8 (&wx)[8],
;         float ba, float bxx, float sp8, int r, int hh, int chl, float& st, float& CA, float& CB) {
;     ...
;         for (int bi = 0; bi < 2; ++bi) { const int tb = z ? 1 - bi : bi;
;             if (z == 1 && bi == 0) __builtin_amdgcn_s_sleep(8);
;             f32x16 ya, yx;
; #pragma unroll
;             for (int i = 0; i < 16; ++i) { ya[i] = ba; yx[i] = bxx; }
; #pragma unroll
;             for (int s = 0; s < 8; ++s) { const bf16x8 af = *(const LAS bf16x8*)(XCB + (32 * tb + r) * 272 + (16 * s + 8 * hh) * 2);
;                 ya = __builtin_amdgcn_mfma_f32_32x32x16_bf16(af, wa[s], ya, 0, 0, 0); yx = __builtin_amdgcn_mfma_f32_32x32x16_bf16(af, wx[s], yx, 0, 0, 0); }
;             float av[16], bv[16];
; #pragma unroll
;             for (int i = 0; i < 16; i += 2) {
;                 typedef float f2 __attribute__((ext_vector_type(2)));
;                 const f2 xc = {XCF[(32 * tb + crow(i, hh)) * 128 + chl], XCF[(32 * tb + crow(i + 1, hh)) * 128 + chl]};
;                 const f2 ta = (f2){ya[i], ya[i + 1]} * -1.4426950408889634f, tx = (f2){yx[i], yx[i + 1]} * -1.4426950408889634f;
;                 f2 ea, ex; ea.x = __builtin_amdgcn_exp2f(ta.x); ea.y = __builtin_amdgcn_exp2f(ta.y); ex.x = __builtin_amdgcn_exp2f(tx.x); ex.y = __builtin_amdgcn_exp2f(tx.y);
;                 const f2 da = ea + 1.0f, dx = ex + 1.0f;
;                 f2 rg, ig; rg.x = __builtin_amdgcn_rcpf(da.x); rg.y = __builtin_amdgcn_rcpf(da.y); ig.x = __builtin_amdgcn_rcpf(dx.x); ig.y = __builtin_amdgcn_rcpf(dx.y);
;                 const f2 la = rg * sp8; f2 a; a.x = __builtin_amdgcn_exp2f(la.x); a.y = __builtin_amdgcn_exp2f(la.y);
;                 const f2 om = a * -a + 1.0f; f2 sq; sq.x = __builtin_amdgcn_sqrtf(om.x); sq.y = __builtin_amdgcn_sqrtf(om.y);
;                 const f2 b = sq * ig * xc;
;                 av[i] = a.x; av[i + 1] = a.y; bv[i] = b.x; bv[i + 1] = b.y; }
.LBB0_1410:
	v_and_b32_e32 v35, 64, v184
	v_xor_b32_e32 v34, 32, v184
	v_add_u32_e32 v35, 64, v35
	v_cmp_lt_i32_e32 vcc, v34, v35
	s_mov_b64 s[6:7], -1
	s_nop 0
	v_cndmask_b32_e32 v34, v184, v34, vcc
	v_lshlrev_b32_e32 v155, 2, v34
	s_and_b64 vcc, exec, s[16:17]
	s_cbranch_vccz .LBB0_1441
	s_sleep 16
	ds_read_b128 v[170:173], v185 offset:8704
	ds_read_b128 v[188:191], v185 offset:8736
	s_waitcnt lgkmcnt(1)
	v_mfma_f32_32x32x16_bf16 v[50:65], v[170:173], v[66:69], v[2:17]
	v_mfma_f32_32x32x16_bf16 v[34:49], v[170:173], v[98:101], v[18:33]
	s_waitcnt lgkmcnt(0)
	v_mfma_f32_32x32x16_bf16 v[50:65], v[188:191], v[70:73], v[50:65]
	v_mfma_f32_32x32x16_bf16 v[34:49], v[188:191], v[102:105], v[34:49]
	ds_read_b128 v[170:173], v185 offset:8768
	ds_read_b128 v[188:191], v185 offset:8800
	s_waitcnt lgkmcnt(1)
	v_mfma_f32_32x32x16_bf16 v[50:65], v[170:173], v[74:77], v[50:65]
	v_mfma_f32_32x32x16_bf16 v[34:49], v[170:173], v[106:109], v[34:49]
	s_waitcnt lgkmcnt(0)
	v_mfma_f32_32x32x16_bf16 v[50:65], v[188:191], v[78:81], v[50:65]
	v_mfma_f32_32x32x16_bf16 v[34:49], v[188:191], v[110:113], v[34:49]
	ds_read_b128 v[170:173], v185 offset:8832
	ds_read_b128 v[188:191], v185 offset:8864
	s_waitcnt lgkmcnt(1)
	v_mfma_f32_32x32x16_bf16 v[50:65], v[170:173], v[82:85], v[50:65]
	v_mfma_f32_32x32x16_bf16 v[34:49], v[170:173], v[114:117], v[34:49]
	s_waitcnt lgkmcnt(0)
	v_mfma_f32_32x32x16_bf16 v[50:65], v[188:191], v[86:89], v[50:65]
	v_mfma_f32_32x32x16_bf16 v[34:49], v[188:191], v[118:121], v[34:49]
	ds_read_b128 v[170:173], v185 offset:8896
	ds_read_b128 v[188:191], v185 offset:8928
	ds_read2st64_b32 v[192:193], v186 offset0:168 offset1:170
	ds_read2st64_b32 v[196:197], v186 offset0:180 offset1:182
	s_waitcnt lgkmcnt(3)
	v_mfma_f32_32x32x16_bf16 v[50:65], v[170:173], v[90:93], v[50:65]
	s_waitcnt lgkmcnt(2)
	v_mfma_f32_32x32x16_bf16 v[50:65], v[188:191], v[94:97], v[50:65]
	v_mfma_f32_32x32x16_bf16 v[34:49], v[170:173], v[122:125], v[34:49]
	s_nop 10
	v_mul_f32_e64 v50, v50, s20
	v_mul_f32_e64 v51, v51, s20
	v_mul_f32_e64 v56, v56, s20
	v_mul_f32_e64 v57, v57, s20
	v_exp_f32_e32 v50, v50
	v_exp_f32_e32 v51, v51
	v_exp_f32_e32 v56, v56
	v_exp_f32_e32 v57, v57
	v_pk_mul_f32 v[54:55], v[54:55], s[20:21] op_sel_hi:[1,0]
	v_pk_add_f32 v[50:51], v[50:51], 1.0 op_sel_hi:[1,0]
	v_mfma_f32_32x32x16_bf16 v[34:49], v[188:191], v[126:129], v[34:49]
	v_rcp_f32_e32 v172, v50
	v_rcp_f32_e32 v173, v51
	v_pk_mul_f32 v[50:51], v[52:53], s[20:21] op_sel_hi:[1,0]
	v_pk_add_f32 v[56:57], v[56:57], 1.0 op_sel_hi:[1,0]
	v_exp_f32_e32 v52, v50
	v_exp_f32_e32 v53, v51
	v_rcp_f32_e32 v56, v56
	s_nop 4
	v_pk_mul_f32 v[34:35], v[34:35], s[20:21] op_sel_hi:[1,0]
	v_pk_mul_f32 v[36:37], v[36:37], s[20:21] op_sel_hi:[1,0]
	v_pk_add_f32 v[52:53], v[52:53], 1.0 op_sel_hi:[1,0]
	v_exp_f32_e32 v170, v34
	v_rcp_f32_e32 v52, v52
	v_rcp_f32_e32 v53, v53
	v_exp_f32_e32 v171, v35
	v_exp_f32_e32 v36, v36
	v_exp_f32_e32 v37, v37
	v_pk_mul_f32 v[52:53], v[164:165], v[52:53]
	v_pk_add_f32 v[170:171], v[170:171], 1.0 op_sel_hi:[1,0]
	v_exp_f32_e32 v52, v52
	v_exp_f32_e32 v53, v53
	v_pk_add_f32 v[36:37], v[36:37], 1.0 op_sel_hi:[1,0]
	v_rcp_f32_e32 v50, v170
	v_rcp_f32_e32 v51, v171
	v_pk_mul_f32 v[170:171], v[164:165], v[172:173]
	v_rcp_f32_e32 v172, v36
	v_rcp_f32_e32 v173, v37
	v_pk_fma_f32 v[36:37], v[52:53], v[52:53], 1.0 op_sel_hi:[1,1,0] neg_lo:[1,0,0] neg_hi:[1,0,0]
	v_rcp_f32_e32 v57, v57
	v_sqrt_f32_e32 v174, v36
	v_sqrt_f32_e32 v175, v37
	v_exp_f32_e32 v36, v170
	v_exp_f32_e32 v37, v171
	ds_read2st64_b32 v[170:171], v186 offset0:136 offset1:138
	v_pk_mul_f32 v[38:39], v[38:39], s[20:21] op_sel_hi:[1,0]
	v_pk_mul_f32 v[40:41], v[40:41], s[20:21] op_sel_hi:[1,0]
	v_pk_mul_f32 v[56:57], v[164:165], v[56:57]
	v_pk_mul_f32 v[172:173], v[172:173], v[174:175]
	v_exp_f32_e32 v174, v54
	v_exp_f32_e32 v175, v55
	v_exp_f32_e32 v38, v38
	v_exp_f32_e32 v39, v39
	v_exp_f32_e32 v40, v40
	v_exp_f32_e32 v41, v41
	v_exp_f32_e32 v56, v56
	v_exp_f32_e32 v57, v57
	s_waitcnt lgkmcnt(0)
	v_pk_mul_f32 v[170:171], v[170:171], v[172:173]
	v_pk_add_f32 v[172:173], v[174:175], 1.0 op_sel_hi:[1,0]
	v_pk_add_f32 v[38:39], v[38:39], 1.0 op_sel_hi:[1,0]
	v_pk_add_f32 v[40:41], v[40:41], 1.0 op_sel_hi:[1,0]
	v_pk_fma_f32 v[188:189], v[56:57], v[56:57], 1.0 op_sel_hi:[1,1,0] neg_lo:[1,0,0] neg_hi:[1,0,0]
	v_rcp_f32_e32 v172, v172
	v_rcp_f32_e32 v173, v173
	v_rcp_f32_e32 v174, v38
	v_rcp_f32_e32 v175, v39
	ds_read2st64_b32 v[38:39], v186 offset0:152 offset1:154
	v_rcp_f32_e32 v40, v40
	v_rcp_f32_e32 v41, v41
	v_sqrt_f32_e32 v188, v188
	v_sqrt_f32_e32 v189, v189
	v_pk_mul_f32 v[172:173], v[164:165], v[172:173]
	ds_read2st64_b32 v[34:35], v186 offset0:132 offset1:134
	v_exp_f32_e32 v191, v172
	v_pk_mul_f32 v[40:41], v[40:41], v[188:189]
	v_exp_f32_e32 v190, v173
	s_waitcnt lgkmcnt(1)
; template <bool FINAL, int z> __device__ __forceinline__ void rglru_blocks(LAS unsigned char* XCB, LAS float* XCF, LAS float* HS, const bf16x8 (&wa)[8], const bf16x8 (&wx)[8],
;         float ba, float bxx, float sp8, int r, int hh, int chl, float& st, float& CA, float& CB) {
;     ...
;                 const f2 ta = (f2){ya[i], ya[i + 1]} * -1.4426950408889634f, tx = (f2){yx[i], yx[i + 1]} * -1.4426950408889634f;
;                 f2 ea, ex; ea.x = __builtin_amdgcn_exp2f(ta.x); ea.y = __builtin_amdgcn_exp2f(ta.y); ex.x = __builtin_amdgcn_exp2f(tx.x); ex.y = __builtin_amdgcn_exp2f(tx.y);
;                 const f2 da = ea + 1.0f, dx = ex + 1.0f;
;                 f2 rg, ig; rg.x = __builtin_amdgcn_rcpf(da.x); rg.y = __builtin_amdgcn_rcpf(da.y); ig.x = __builtin_amdgcn_rcpf(dx.x); ig.y = __builtin_amdgcn_rcpf(dx.y);
;                 const f2 la = rg * sp8; f2 a; a.x = __builtin_amdgcn_exp2f(la.x); a.y = __builtin_amdgcn_exp2f(la.y);
;                 const f2 om = a * -a + 1.0f; f2 sq; sq.x = __builtin_amdgcn_sqrtf(om.x); sq.y = __builtin_amdgcn_sqrtf(om.y);
;                 const f2 b = sq * ig * xc;
;                 av[i] = a.x; av[i + 1] = a.y; bv[i] = b.x; bv[i + 1] = b.y; }
;             float Ag[4], Bg[4], Ap[4], Bp[4];
; #pragma unroll
;             for (int g = 0; g < 4; ++g) { float A = 1.f, B = 0.f;
; #pragma unroll
;                 for (int k = 0; k < 4; ++k) { const int kk = z ? 3 - k : k; B = B * av[4 * g + kk] + bv[4 * g + kk]; A *= av[4 * g + kk]; }
;                 Ag[g] = A; Bg[g] = B; Ap[g] = __shfl_xor(A, 32); Bp[g] = __shfl_xor(B, 32); }
;             float ent[4]; float cur = st;
; #pragma unroll
;             for (int gi = 0; gi < 4; ++gi) { const int g = z ? 3 - gi : gi;
;                 const bool own_first = z ? (hh == 1) : (hh == 0);
;                 if (own_first) { ent[g] = cur; cur = Ag[g] * cur + Bg[g]; CB = Ag[g] * CB + Bg[g]; CA *= Ag[g]; cur = Ap[g] * cur + Bp[g]; CB = Ap[g] * CB + Bp[g]; CA *= Ap[g]; }
;                 else { cur = Ap[g] * cur + Bp[g]; CB = Ap[g] * CB + Bp[g]; CA *= Ap[g]; ent[g] = cur; cur = Ag[g] * cur + Bg[g]; CB = Ag[g] * CB + Bg[g]; CA *= Ag[g]; } }
	v_pk_mul_f32 v[172:173], v[38:39], v[40:41]
	v_pk_mul_f32 v[38:39], v[58:59], s[20:21] op_sel_hi:[1,0]
	v_pk_mul_f32 v[40:41], v[42:43], s[20:21] op_sel_hi:[1,0]
	v_exp_f32_e32 v38, v38
	v_exp_f32_e32 v39, v39
	v_exp_f32_e32 v40, v40
	v_exp_f32_e32 v41, v41
	v_pk_mul_f32 v[42:43], v[44:45], s[20:21] op_sel_hi:[1,0]
	v_pk_add_f32 v[38:39], v[38:39], 1.0 op_sel_hi:[1,0]
	v_exp_f32_e32 v42, v42
	v_rcp_f32_e32 v38, v38
	v_rcp_f32_e32 v39, v39
	v_pk_add_f32 v[40:41], v[40:41], 1.0 op_sel_hi:[1,0]
	v_exp_f32_e32 v43, v43
	v_rcp_f32_e32 v58, v40
	v_rcp_f32_e32 v59, v41
	v_pk_mul_f32 v[40:41], v[164:165], v[38:39]
	v_pk_add_f32 v[42:43], v[42:43], 1.0 op_sel_hi:[1,0]
	v_exp_f32_e32 v39, v40
	v_exp_f32_e32 v38, v41
	v_pk_mul_f32 v[40:41], v[60:61], s[20:21] op_sel_hi:[1,0]
	v_rcp_f32_e32 v60, v42
	v_exp_f32_e32 v40, v40
	v_exp_f32_e32 v41, v41
	v_rcp_f32_e32 v61, v43
	v_pk_mul_f32 v[42:43], v[62:63], s[20:21] op_sel_hi:[1,0]
	v_pk_mul_f32 v[44:45], v[46:47], s[20:21] op_sel_hi:[1,0]
	v_pk_add_f32 v[40:41], v[40:41], 1.0 op_sel_hi:[1,0]
	v_exp_f32_e32 v42, v42
	v_rcp_f32_e32 v40, v40
	v_rcp_f32_e32 v41, v41
	v_exp_f32_e32 v43, v43
	v_exp_f32_e32 v44, v44
	v_exp_f32_e32 v45, v45
	v_pk_mul_f32 v[40:41], v[164:165], v[40:41]
	v_pk_mul_f32 v[46:47], v[48:49], s[20:21] op_sel_hi:[1,0]
	v_exp_f32_e32 v194, v40
	v_exp_f32_e32 v63, v41
	v_pk_add_f32 v[40:41], v[42:43], 1.0 op_sel_hi:[1,0]
	v_pk_add_f32 v[42:43], v[44:45], 1.0 op_sel_hi:[1,0]
	v_pk_mul_f32 v[44:45], v[64:65], s[20:21] op_sel_hi:[1,0]
	v_exp_f32_e32 v46, v46
	v_exp_f32_e32 v44, v44
	v_exp_f32_e32 v45, v45
	v_exp_f32_e32 v47, v47
	v_rcp_f32_e32 v40, v40
	v_rcp_f32_e32 v41, v41
	v_pk_add_f32 v[44:45], v[44:45], 1.0 op_sel_hi:[1,0]
	v_rcp_f32_e32 v64, v42
	v_rcp_f32_e32 v44, v44
	v_rcp_f32_e32 v45, v45
	v_rcp_f32_e32 v65, v43
	ds_read2st64_b32 v[42:43], v186 offset0:184 offset1:186
	v_pk_mul_f32 v[40:41], v[164:165], v[40:41]
	v_pk_mul_f32 v[44:45], v[164:165], v[44:45]
	v_exp_f32_e32 v198, v40
	v_exp_f32_e32 v48, v44
	v_exp_f32_e32 v49, v45
	v_pk_add_f32 v[44:45], v[46:47], 1.0 op_sel_hi:[1,0]
	v_exp_f32_e32 v62, v41
	v_rcp_f32_e32 v44, v44
	v_pk_fma_f32 v[46:47], v[48:49], v[48:49], 1.0 op_sel_hi:[1,1,0] neg_lo:[1,0,0] neg_hi:[1,0,0]
	v_rcp_f32_e32 v45, v45
	v_sqrt_f32_e32 v46, v46
	v_sqrt_f32_e32 v47, v47
	ds_read2st64_b32 v[54:55], v186 offset0:148 offset1:150
	v_mov_b32_e32 v195, v63
	ds_read2st64_b32 v[188:189], v186 offset0:164 offset1:166
	v_pk_mul_f32 v[40:41], v[44:45], v[46:47]
	v_mov_b32_e32 v199, v38
	s_waitcnt lgkmcnt(2)
	v_pk_mul_f32 v[200:201], v[42:43], v[40:41]
	v_pk_fma_f32 v[40:41], v[36:37], v[36:37], 1.0 op_sel_hi:[1,1,0] neg_lo:[1,0,0] neg_hi:[1,0,0]
	v_fma_f32 v42, 0, v53, v171
	v_sqrt_f32_e32 v40, v40
	v_sqrt_f32_e32 v41, v41
	v_fmac_f32_e32 v170, v52, v42
	v_mul_f32_e32 v43, v53, v52
	v_pk_mul_f32 v[40:41], v[50:51], v[40:41]
	s_nop 0
	v_pk_mul_f32 v[40:41], v[34:35], v[40:41]
	s_nop 0
	v_fma_f32 v42, v37, v170, v41
	v_mov_b32_e32 v41, v36
	v_pk_mul_f32 v[44:45], v[36:37], v[42:43]
	v_pk_fma_f32 v[34:35], v[36:37], v[42:43], v[40:41]
	v_pk_fma_f32 v[42:43], v[190:191], v[190:191], 1.0 op_sel_hi:[1,1,0] neg_lo:[1,0,0] neg_hi:[1,0,0]
	v_pk_mul_f32 v[40:41], v[40:41], v[44:45]
	v_sqrt_f32_e32 v44, v43
	v_sqrt_f32_e32 v45, v42
	v_fma_f32 v35, 0, v57, v173
	v_fmac_f32_e32 v172, v56, v35
	v_mul_f32_e32 v42, v57, v56
	v_pk_mul_f32 v[44:45], v[174:175], v[44:45]
	v_fma_f32 v35, 0, v49, v201
	s_waitcnt lgkmcnt(1)
	v_pk_mul_f32 v[44:45], v[54:55], v[44:45]
	v_mov_b32_e32 v54, v198
	v_fma_f32 v43, v190, v172, v45
	v_pk_mul_f32 v[46:47], v[190:191], v[42:43]
	v_pk_mov_b32 v[50:51], v[190:191], v[44:45] op_sel:[1,0]
	v_mov_b32_e32 v55, v62
	v_pk_fma_f32 v[44:45], v[190:191], v[42:43], v[50:51]
	v_pk_mul_f32 v[46:47], v[50:51], v[46:47]
	v_pk_fma_f32 v[50:51], v[38:39], v[38:39], 1.0 op_sel_hi:[1,1,0] neg_lo:[1,0,0] neg_hi:[1,0,0]
	v_pk_fma_f32 v[54:55], v[54:55], v[54:55], 1.0 op_sel_hi:[1,1,0] neg_lo:[1,0,0] neg_hi:[1,0,0]
	v_sqrt_f32_e32 v52, v51
	v_sqrt_f32_e32 v53, v50
	v_sqrt_f32_e32 v54, v54
	v_sqrt_f32_e32 v55, v55
	v_fmac_f32_e32 v200, v48, v35
	v_pk_mul_f32 v[50:51], v[58:59], v[52:53]
	v_pk_fma_f32 v[52:53], v[194:195], v[194:195], 1.0 op_sel_hi:[1,1,0] neg_lo:[1,0,0] neg_hi:[1,0,0]
	s_waitcnt lgkmcnt(0)
	v_pk_mul_f32 v[56:57], v[188:189], v[50:51]
	v_sqrt_f32_e32 v52, v52
	v_sqrt_f32_e32 v53, v53
	v_mul_f32_e32 v48, v49, v48
	v_mov_b32_e32 v49, v194
	v_pk_mul_f32 v[48:49], v[62:63], v[48:49]
	v_pk_mul_f32 v[50:51], v[60:61], v[52:53]
	v_pk_mul_f32 v[60:61], v[198:199], v[48:49]
	v_pk_mul_f32 v[52:53], v[192:193], v[50:51]
	v_pk_mul_f32 v[50:51], v[64:65], v[54:55]
	v_fma_f32 v35, 0, v63, v53
	v_fmac_f32_e32 v52, v194, v35
	v_pk_mul_f32 v[50:51], v[196:197], v[50:51]
	v_fma_f32 v53, v38, v52, v57
	v_mov_b32_e32 v52, v49
	v_pk_mul_f32 v[54:55], v[38:39], v[52:53]
	v_pk_mov_b32 v[48:49], v[38:39], v[56:57] op_sel:[1,0]
	v_fma_f32 v35, v62, v200, v51
	v_pk_fma_f32 v[56:57], v[38:39], v[52:53], v[48:49]
	v_pk_mul_f32 v[52:53], v[48:49], v[54:55]
	ds_bpermute_b32 v38, v155, v60
	v_fmac_f32_e32 v50, v198, v35
	ds_bpermute_b32 v37, v155, v41
	ds_bpermute_b32 v36, v155, v34
	ds_bpermute_b32 v42, v155, v46
	ds_bpermute_b32 v43, v155, v45
	ds_bpermute_b32 v54, v155, v52
	ds_bpermute_b32 v55, v155, v57
	ds_bpermute_b32 v35, v155, v50
	v_mov_b32_e32 v53, v57
	s_waitcnt lgkmcnt(7)
	v_pk_mul_f32 v[58:59], v[38:39], v[60:61]
	s_and_saveexec_b64 s[6:7], s[0:1]
	s_xor_b64 s[6:7], exec, s[6:7]
	s_cbranch_execz .LBB0_1413
	s_waitcnt lgkmcnt(0)
	v_fmac_f32_e32 v35, 0, v38
	v_fmac_f32_e32 v50, v60, v35
	v_mov_b32_e32 v39, v55
	v_fmac_f32_e32 v39, v50, v54
	v_mov_b32_e32 v38, v54
	v_pk_mul_f32 v[50:51], v[58:59], v[54:55]
	v_pk_fma_f32 v[48:49], v[58:59], v[38:39], v[52:53]
	s_nop 0
	v_mul_f32_e32 v48, v52, v50

; template <bool FINAL, int z> __device__ __forceinline__ void rglru_blocks(LAS unsigned char* XCB, LAS float* XCF, LAS float* HS, const bf16x8 (&wa)[8], const bf16x8 (&wx)[8],
;         float ba, float bxx, float sp8, int r, int hh, int chl, float& st, float& CA, float& CB) {
;     ...
;         for (int bi = 0; bi < 2; ++bi) { const int tb = z ? 1 - bi : bi;
;             if (z == 1 && bi == 0) __builtin_amdgcn_s_sleep(8);
;             f32x16 ya, yx;
; #pragma unroll
;             for (int i = 0; i < 16; ++i) { ya[i] = ba; yx[i] = bxx; }
; #pragma unroll
;             for (int s = 0; s < 8; ++s) { const bf16x8 af = *(const LAS bf16x8*)(XCB + (32 * tb + r) * 272 + (16 * s + 8 * hh) * 2);
;                 ya = __builtin_amdgcn_mfma_f32_32x32x16_bf16(af, wa[s], ya, 0, 0, 0); yx = __builtin_amdgcn_mfma_f32_32x32x16_bf16(af, wx[s], yx, 0, 0, 0); }
;             float av[16], bv[16];
; #pragma unroll
;             for (int i = 0; i < 16; i += 2) {
;                 typedef float f2 __attribute__((ext_vector_type(2)));
;                 const f2 xc = {XCF[(32 * tb + crow(i, hh)) * 128 + chl], XCF[(32 * tb + crow(i + 1, hh)) * 128 + chl]};
;                 const f2 ta = (f2){ya[i], ya[i + 1]} * -1.4426950408889634f, tx = (f2){yx[i], yx[i + 1]} * -1.4426950408889634f;
;                 f2 ea, ex; ea.x = __builtin_amdgcn_exp2f(ta.x); ea.y = __builtin_amdgcn_exp2f(ta.y); ex.x = __builtin_amdgcn_exp2f(tx.x); ex.y = __builtin_amdgcn_exp2f(tx.y);
;                 const f2 da = ea + 1.0f, dx = ex + 1.0f;
;                 f2 rg, ig; rg.x = __builtin_amdgcn_rcpf(da.x); rg.y = __builtin_amdgcn_rcpf(da.y); ig.x = __builtin_amdgcn_rcpf(dx.x); ig.y = __builtin_amdgcn_rcpf(dx.y);
;                 const f2 la = rg * sp8; f2 a; a.x = __builtin_amdgcn_exp2f(la.x); a.y = __builtin_amdgcn_exp2f(la.y);
;                 const f2 om = a * -a + 1.0f; f2 sq; sq.x = __builtin_amdgcn_sqrtf(om.x); sq.y = __builtin_amdgcn_sqrtf(om.y);
;                 const f2 b = sq * ig * xc;
; template <bool FINAL> __device__ __forceinline__ void rglru_pass(Frame& F) {
;     ...
;         if (FINAL) {
; #pragma unroll
;             for (int it = 0; it < 2; ++it) { const int id = F.tid + 512 * it; gq[it] = *(const GAS v4u*)(Z1 + (size_t)(row0 + (id >> 4)) * 4096 + h * 128 + (id & 15) * 8); } }
;         float st = 0.f, CA = 1.f, CB = 0.f;
;         if (FINAL) st = CL[((c - cg) / ncg) * 256 + z * 128 + chl];
.LBB0_1603:
	v_add_u32_e32 v192, s15, v174
	v_ashrrev_i32_e32 v193, 31, v192
	v_add_u32_e32 v190, s15, v176
	v_lshlrev_b64 v[34:35], 13, v[192:193]
	v_ashrrev_i32_e32 v191, 31, v190
	v_lshl_add_u64 v[34:35], v[188:189], 0, v[34:35]
	v_lshlrev_b64 v[36:37], 13, v[190:191]
	v_lshl_add_u64 v[36:37], v[188:189], 0, v[36:37]
	global_load_dwordx4 v[168:171], v[34:35], off
	global_load_dwordx4 v[164:167], v[36:37], off
	s_abs_i32 s5, s22
	s_mul_hi_u32 s23, s5, s16
	s_mul_i32 s24, s23, s13
	s_ashr_i32 s4, s22, 31
	s_sub_i32 s5, s5, s24
	s_xor_b32 s4, s4, s14
	s_add_i32 s24, s23, 1
	s_sub_i32 s25, s5, s13
	s_cmp_ge_u32 s5, s13
	s_cselect_b32 s23, s24, s23
	s_cselect_b32 s5, s25, s5
	s_add_i32 s24, s23, 1
	s_cmp_ge_u32 s5, s13
	s_cselect_b32 s5, s24, s23
	s_xor_b32 s5, s5, s4
	s_sub_i32 s4, s5, s4
	v_lshl_add_u32 v34, s4, 10, v1
	ds_read_b32 v209, v34
	v_and_b32_e32 v35, 64, v203
	v_xor_b32_e32 v34, 32, v203
	v_add_u32_e32 v35, 64, v35
	v_cmp_lt_i32_e32 vcc, v34, v35
	s_mov_b64 s[4:5], -1
	s_nop 0
	v_cndmask_b32_e32 v34, v203, v34, vcc
	v_lshlrev_b32_e32 v159, 2, v34
	s_and_b64 vcc, exec, s[8:9]
	s_cbranch_vccz .LBB0_1605
	s_sleep 16
	ds_read_b128 v[210:213], v208 offset:8704
	ds_read_b128 v[214:217], v208 offset:8736
	s_mov_b64 s[4:5], 0
	s_waitcnt lgkmcnt(1)
	v_mfma_f32_32x32x16_bf16 v[50:65], v[210:213], v[66:69], v[2:17]
	v_mfma_f32_32x32x16_bf16 v[34:49], v[210:213], v[98:101], v[18:33]
	s_waitcnt lgkmcnt(0)
	v_mfma_f32_32x32x16_bf16 v[50:65], v[214:217], v[70:73], v[50:65]
	v_mfma_f32_32x32x16_bf16 v[34:49], v[214:217], v[102:105], v[34:49]
	ds_read_b128 v[210:213], v208 offset:8768
	ds_read_b128 v[214:217], v208 offset:8800
	s_waitcnt lgkmcnt(1)
	v_mfma_f32_32x32x16_bf16 v[50:65], v[210:213], v[74:77], v[50:65]
	v_mfma_f32_32x32x16_bf16 v[34:49], v[210:213], v[106:109], v[34:49]
	s_waitcnt lgkmcnt(0)
	v_mfma_f32_32x32x16_bf16 v[50:65], v[214:217], v[78:81], v[50:65]
	v_mfma_f32_32x32x16_bf16 v[34:49], v[214:217], v[110:113], v[34:49]
	ds_read_b128 v[210:213], v208 offset:8832
	ds_read_b128 v[214:217], v208 offset:8864
	s_waitcnt lgkmcnt(1)
	v_mfma_f32_32x32x16_bf16 v[50:65], v[210:213], v[82:85], v[50:65]
	v_mfma_f32_32x32x16_bf16 v[34:49], v[210:213], v[114:117], v[34:49]
	s_waitcnt lgkmcnt(0)
	v_mfma_f32_32x32x16_bf16 v[50:65], v[214:217], v[86:89], v[50:65]
	v_mfma_f32_32x32x16_bf16 v[34:49], v[214:217], v[118:121], v[34:49]
	ds_read_b128 v[210:213], v208 offset:8896
	ds_read_b128 v[214:217], v208 offset:8928
	s_waitcnt lgkmcnt(1)
	v_mfma_f32_32x32x16_bf16 v[50:65], v[210:213], v[90:93], v[50:65]
	s_waitcnt lgkmcnt(0)
	v_mfma_f32_32x32x16_bf16 v[50:65], v[214:217], v[94:97], v[50:65]
	v_mfma_f32_32x32x16_bf16 v[34:49], v[210:213], v[122:125], v[34:49]
	s_nop 10
	v_mul_f32_e64 v50, v50, s12
	v_mul_f32_e64 v51, v51, s12
	v_mul_f32_e64 v54, v54, s12
	v_mul_f32_e64 v55, v55, s12
	v_exp_f32_e32 v50, v50
	v_exp_f32_e32 v51, v51
	v_pk_mul_f32 v[52:53], v[52:53], s[12:13] op_sel_hi:[1,0]
	v_exp_f32_e32 v54, v54
	v_exp_f32_e32 v55, v55
	v_mfma_f32_32x32x16_bf16 v[34:49], v[214:217], v[126:129], v[34:49]
	v_add_f32_e64 v50, v50, 1.0
	v_add_f32_e64 v51, v51, 1.0
	v_exp_f32_e32 v52, v52
	v_rcp_f32_e32 v50, v50
	v_rcp_f32_e32 v51, v51
	v_exp_f32_e32 v53, v53
	v_pk_add_f32 v[54:55], v[54:55], 1.0 op_sel_hi:[1,0]
	ds_read2st64_b32 v[210:211], v175 offset0:132 offset1:134
	s_nop 3
	v_pk_mul_f32 v[34:35], v[34:35], s[12:13] op_sel_hi:[1,0]
	v_pk_add_f32 v[52:53], v[52:53], 1.0 op_sel_hi:[1,0]
	v_exp_f32_e32 v212, v34
	v_exp_f32_e32 v213, v35
	v_pk_mul_f32 v[34:35], v[182:183], v[50:51]
	v_rcp_f32_e32 v54, v54
	v_exp_f32_e32 v34, v34
	v_exp_f32_e32 v35, v35
	v_pk_add_f32 v[50:51], v[212:213], 1.0 op_sel_hi:[1,0]
	v_rcp_f32_e32 v55, v55
	v_rcp_f32_e32 v50, v50
	v_pk_fma_f32 v[212:213], v[34:35], v[34:35], 1.0 op_sel_hi:[1,1,0] neg_lo:[1,0,0] neg_hi:[1,0,0]
	v_rcp_f32_e32 v51, v51
	v_sqrt_f32_e32 v212, v212
	v_sqrt_f32_e32 v213, v213
	v_rcp_f32_e32 v52, v52
	v_rcp_f32_e32 v53, v53
	v_pk_mul_f32 v[38:39], v[38:39], s[12:13] op_sel_hi:[1,0]
	v_pk_mul_f32 v[50:51], v[50:51], v[212:213]
	v_pk_mul_f32 v[36:37], v[36:37], s[12:13] op_sel_hi:[1,0]
	v_exp_f32_e32 v214, v38
	v_exp_f32_e32 v215, v39
	v_pk_mul_f32 v[38:39], v[182:183], v[54:55]
	s_waitcnt lgkmcnt(0)
	v_pk_mul_f32 v[50:51], v[210:211], v[50:51]
	v_exp_f32_e32 v210, v36
	v_exp_f32_e32 v211, v37
	v_pk_mul_f32 v[36:37], v[182:183], v[52:53]
	v_exp_f32_e32 v38, v38
	v_exp_f32_e32 v39, v39
	v_exp_f32_e32 v36, v36
	v_exp_f32_e32 v37, v37
	v_pk_add_f32 v[54:55], v[214:215], 1.0 op_sel_hi:[1,0]
	v_pk_add_f32 v[52:53], v[210:211], 1.0 op_sel_hi:[1,0]
	v_rcp_f32_e32 v214, v54
	v_rcp_f32_e32 v215, v55
	v_pk_fma_f32 v[54:55], v[38:39], v[38:39], 1.0 op_sel_hi:[1,1,0] neg_lo:[1,0,0] neg_hi:[1,0,0]
	v_pk_fma_f32 v[210:211], v[36:37], v[36:37], 1.0 op_sel_hi:[1,1,0] neg_lo:[1,0,0] neg_hi:[1,0,0]
	v_sqrt_f32_e32 v216, v54
	v_sqrt_f32_e32 v217, v55
	v_pk_mul_f32 v[54:55], v[56:57], s[12:13] op_sel_hi:[1,0]
	v_rcp_f32_e32 v52, v52
	v_rcp_f32_e32 v53, v53
	v_sqrt_f32_e32 v210, v210
	v_sqrt_f32_e32 v211, v211
	v_exp_f32_e32 v56, v54
	v_exp_f32_e32 v57, v55
	ds_read2st64_b32 v[212:213], v175 offset0:136 offset1:138
	v_pk_mul_f32 v[58:59], v[58:59], s[12:13] op_sel_hi:[1,0]
	v_pk_mul_f32 v[52:53], v[52:53], v[210:211]
	ds_read2st64_b32 v[210:211], v175 offset0:148 offset1:150
	v_pk_add_f32 v[56:57], v[56:57], 1.0 op_sel_hi:[1,0]
	v_exp_f32_e32 v58, v58
	v_exp_f32_e32 v59, v59
	v_rcp_f32_e32 v56, v56
	v_rcp_f32_e32 v57, v57
	s_waitcnt lgkmcnt(1)
	v_pk_mul_f32 v[54:55], v[212:213], v[52:53]
	v_pk_mul_f32 v[52:53], v[214:215], v[216:217]
	v_pk_mul_f32 v[40:41], v[40:41], s[12:13] op_sel_hi:[1,0]
	v_pk_add_f32 v[58:59], v[58:59], 1.0 op_sel_hi:[1,0]
	s_waitcnt lgkmcnt(0)
; template <bool FINAL, int z> __device__ __forceinline__ void rglru_blocks(LAS unsigned char* XCB, LAS float* XCF, LAS float* HS, const bf16x8 (&wa)[8], const bf16x8 (&wx)[8],
;         float ba, float bxx, float sp8, int r, int hh, int chl, float& st, float& CA, float& CB) {
;     ...
;                 const f2 ta = (f2){ya[i], ya[i + 1]} * -1.4426950408889634f, tx = (f2){yx[i], yx[i + 1]} * -1.4426950408889634f;
;                 f2 ea, ex; ea.x = __builtin_amdgcn_exp2f(ta.x); ea.y = __builtin_amdgcn_exp2f(ta.y); ex.x = __builtin_amdgcn_exp2f(tx.x); ex.y = __builtin_amdgcn_exp2f(tx.y);
;                 const f2 da = ea + 1.0f, dx = ex + 1.0f;
;                 f2 rg, ig; rg.x = __builtin_amdgcn_rcpf(da.x); rg.y = __builtin_amdgcn_rcpf(da.y); ig.x = __builtin_amdgcn_rcpf(dx.x); ig.y = __builtin_amdgcn_rcpf(dx.y);
;                 const f2 la = rg * sp8; f2 a; a.x = __builtin_amdgcn_exp2f(la.x); a.y = __builtin_amdgcn_exp2f(la.y);
;                 const f2 om = a * -a + 1.0f; f2 sq; sq.x = __builtin_amdgcn_sqrtf(om.x); sq.y = __builtin_amdgcn_sqrtf(om.y);
;                 const f2 b = sq * ig * xc;
;                 av[i] = a.x; av[i + 1] = a.y; bv[i] = b.x; bv[i + 1] = b.y; }
;             float Ag[4], Bg[4], Ap[4], Bp[4];
; #pragma unroll
;             for (int g = 0; g < 4; ++g) { float A = 1.f, B = 0.f;
; #pragma unroll
;                 for (int k = 0; k < 4; ++k) { const int kk = z ? 3 - k : k; B = B * av[4 * g + kk] + bv[4 * g + kk]; A *= av[4 * g + kk]; }
;                 Ag[g] = A; Bg[g] = B; Ap[g] = __shfl_xor(A, 32); Bp[g] = __shfl_xor(B, 32); }
;             float ent[4]; float cur = st;
; #pragma unroll
;             for (int gi = 0; gi < 4; ++gi) { const int g = z ? 3 - gi : gi;
;                 const bool own_first = z ? (hh == 1) : (hh == 0);
;                 if (own_first) { ent[g] = cur; cur = Ag[g] * cur + Bg[g]; CB = Ag[g] * CB + Bg[g]; CA *= Ag[g]; cur = Ap[g] * cur + Bp[g]; CB = Ap[g] * CB + Bp[g]; CA *= Ap[g]; }
;                 else { cur = Ap[g] * cur + Bp[g]; CB = Ap[g] * CB + Bp[g]; CA *= Ap[g]; ent[g] = cur; cur = Ag[g] * cur + Bg[g]; CB = Ag[g] * CB + Bg[g]; CA *= Ag[g]; } }
	v_pk_mul_f32 v[52:53], v[210:211], v[52:53]
	v_exp_f32_e32 v210, v40
	v_exp_f32_e32 v211, v41
	v_pk_mul_f32 v[40:41], v[182:183], v[56:57]
	v_rcp_f32_e32 v58, v58
	v_rcp_f32_e32 v59, v59
	v_pk_mul_f32 v[60:61], v[60:61], s[12:13] op_sel_hi:[1,0]
	v_exp_f32_e32 v40, v40
	v_exp_f32_e32 v41, v41
	v_exp_f32_e32 v60, v60
	v_exp_f32_e32 v61, v61
	v_pk_mul_f32 v[64:65], v[64:65], s[12:13] op_sel_hi:[1,0]
	v_pk_mul_f32 v[42:43], v[42:43], s[12:13] op_sel_hi:[1,0]
	v_exp_f32_e32 v64, v64
	v_exp_f32_e32 v65, v65
	v_exp_f32_e32 v214, v42
	v_exp_f32_e32 v215, v43
	v_pk_mul_f32 v[42:43], v[182:183], v[58:59]
	v_pk_mul_f32 v[62:63], v[62:63], s[12:13] op_sel_hi:[1,0]
	v_pk_add_f32 v[56:57], v[210:211], 1.0 op_sel_hi:[1,0]
	v_pk_fma_f32 v[210:211], v[40:41], v[40:41], 1.0 op_sel_hi:[1,1,0] neg_lo:[1,0,0] neg_hi:[1,0,0]
	v_exp_f32_e32 v42, v42
	v_exp_f32_e32 v43, v43
	v_pk_add_f32 v[60:61], v[60:61], 1.0 op_sel_hi:[1,0]
	v_exp_f32_e32 v62, v62
	v_exp_f32_e32 v63, v63
	v_rcp_f32_e32 v56, v56
	v_rcp_f32_e32 v57, v57
	v_sqrt_f32_e32 v210, v210
	v_sqrt_f32_e32 v211, v211
	v_rcp_f32_e32 v60, v60
	v_rcp_f32_e32 v61, v61
	v_pk_add_f32 v[64:65], v[64:65], 1.0 op_sel_hi:[1,0]
	v_pk_add_f32 v[58:59], v[214:215], 1.0 op_sel_hi:[1,0]
	v_rcp_f32_e32 v64, v64
	v_rcp_f32_e32 v65, v65
	v_pk_fma_f32 v[214:215], v[42:43], v[42:43], 1.0 op_sel_hi:[1,1,0] neg_lo:[1,0,0] neg_hi:[1,0,0]
	v_pk_add_f32 v[62:63], v[62:63], 1.0 op_sel_hi:[1,0]
	v_pk_mul_f32 v[56:57], v[56:57], v[210:211]
	ds_read2st64_b32 v[210:211], v175 offset0:164 offset1:166
	v_rcp_f32_e32 v58, v58
	v_rcp_f32_e32 v59, v59
	v_sqrt_f32_e32 v214, v214
	v_sqrt_f32_e32 v215, v215
	v_pk_mul_f32 v[44:45], v[44:45], s[12:13] op_sel_hi:[1,0]
	v_pk_mul_f32 v[60:61], v[182:183], v[60:61]
	v_rcp_f32_e32 v62, v62
	v_rcp_f32_e32 v63, v63
	v_exp_f32_e32 v44, v44
	v_exp_f32_e32 v45, v45
	v_exp_f32_e32 v60, v60
	v_exp_f32_e32 v61, v61
	v_pk_mul_f32 v[48:49], v[48:49], s[12:13] op_sel_hi:[1,0]
	v_pk_mul_f32 v[64:65], v[182:183], v[64:65]
	v_exp_f32_e32 v48, v48
	v_exp_f32_e32 v49, v49
	v_exp_f32_e32 v64, v64
	v_exp_f32_e32 v65, v65
	v_pk_mul_f32 v[58:59], v[58:59], v[214:215]
	v_pk_mul_f32 v[46:47], v[46:47], s[12:13] op_sel_hi:[1,0]
	v_pk_mul_f32 v[62:63], v[182:183], v[62:63]
	s_waitcnt lgkmcnt(0)
	v_pk_mul_f32 v[58:59], v[210:211], v[58:59]
	v_pk_add_f32 v[44:45], v[44:45], 1.0 op_sel_hi:[1,0]
	v_pk_fma_f32 v[210:211], v[60:61], v[60:61], 1.0 op_sel_hi:[1,1,0] neg_lo:[1,0,0] neg_hi:[1,0,0]
	v_exp_f32_e32 v46, v46
	v_exp_f32_e32 v47, v47
	v_exp_f32_e32 v62, v62
	v_exp_f32_e32 v63, v63
	v_rcp_f32_e32 v44, v44
	v_rcp_f32_e32 v45, v45
	v_sqrt_f32_e32 v210, v210
	v_sqrt_f32_e32 v211, v211
	ds_read2st64_b32 v[212:213], v175 offset0:152 offset1:154
	v_pk_add_f32 v[48:49], v[48:49], 1.0 op_sel_hi:[1,0]
	v_pk_fma_f32 v[218:219], v[64:65], v[64:65], 1.0 op_sel_hi:[1,1,0] neg_lo:[1,0,0] neg_hi:[1,0,0]
	ds_read2st64_b32 v[216:217], v175 offset0:184 offset1:186
	v_rcp_f32_e32 v48, v48
	v_rcp_f32_e32 v49, v49
	v_sqrt_f32_e32 v218, v218
	v_sqrt_f32_e32 v219, v219
	v_pk_add_f32 v[46:47], v[46:47], 1.0 op_sel_hi:[1,0]
	v_pk_fma_f32 v[214:215], v[62:63], v[62:63], 1.0 op_sel_hi:[1,1,0] neg_lo:[1,0,0] neg_hi:[1,0,0]
	v_pk_mul_f32 v[44:45], v[44:45], v[210:211]
	ds_read2st64_b32 v[210:211], v175 offset0:180 offset1:182
	v_rcp_f32_e32 v46, v46
	v_rcp_f32_e32 v47, v47
	v_sqrt_f32_e32 v214, v214
	v_sqrt_f32_e32 v215, v215
	s_waitcnt lgkmcnt(2)
	v_pk_mul_f32 v[56:57], v[212:213], v[56:57]
	ds_read2st64_b32 v[212:213], v175 offset0:168 offset1:170
	v_pk_mul_f32 v[48:49], v[48:49], v[218:219]
	v_pk_mul_f32 v[46:47], v[46:47], v[214:215]
	s_waitcnt lgkmcnt(2)
	v_pk_mul_f32 v[48:49], v[216:217], v[48:49]
	s_waitcnt lgkmcnt(1)
	v_pk_mul_f32 v[46:47], v[210:211], v[46:47]
	v_fma_f32 v218, 0, v65, v49
	v_fma_f32 v218, v64, v218, v48
	v_mul_f32_e32 v219, v65, v64
	v_fma_f32 v218, v63, v218, v47
	v_mul_f32_e32 v219, v63, v219
	s_waitcnt lgkmcnt(0)
	v_pk_mul_f32 v[44:45], v[212:213], v[44:45]
	v_fma_f32 v218, v62, v218, v46
	v_mul_f32_e32 v219, v62, v219
	v_fma_f32 v216, 0, v61, v45
	ds_bpermute_b32 v222, v159, v219
	ds_bpermute_b32 v223, v159, v218
	v_fma_f32 v210, 0, v37, v55
	v_fma_f32 v216, v60, v216, v44
	v_mul_f32_e32 v217, v61, v60
	v_fma_f32 v210, v36, v210, v54
	v_fma_f32 v216, v43, v216, v59
	v_mul_f32_e32 v217, v43, v217
	v_fma_f32 v210, v35, v210, v51
	v_fma_f32 v216, v42, v216, v58
	v_mul_f32_e32 v217, v42, v217
	v_fma_f32 v220, v34, v210, v50
	v_fma_f32 v210, 0, v41, v57
	ds_bpermute_b32 v224, v159, v217
	ds_bpermute_b32 v225, v159, v216
	v_fma_f32 v226, v209, v219, v218
	v_fma_f32 v210, v40, v210, v56
	v_mul_f32_e32 v213, v41, v40
	s_waitcnt lgkmcnt(2)
	v_fma_f32 v226, v226, v222, v223
	v_fmac_f32_e32 v223, v209, v222
	v_fma_f32 v210, v39, v210, v53
	v_mul_f32_e32 v213, v39, v213
	v_fmac_f32_e32 v218, v219, v223
	v_fma_f32 v210, v38, v210, v52
	v_mul_f32_e32 v213, v38, v213
	v_cndmask_b32_e64 v218, v218, v226, s[0:1]
	ds_bpermute_b32 v214, v159, v213
	ds_bpermute_b32 v215, v159, v210
	v_fma_f32 v222, v217, v218, v216
	v_mul_f32_e32 v211, v37, v36
	s_waitcnt lgkmcnt(2)
	v_fma_f32 v222, v222, v224, v225
	v_fmac_f32_e32 v225, v218, v224
	v_mul_f32_e32 v211, v35, v211
	v_fmac_f32_e32 v216, v217, v225
	v_mul_f32_e32 v211, v34, v211
	v_cndmask_b32_e64 v216, v216, v222, s[0:1]
	ds_bpermute_b32 v212, v159, v211
	ds_bpermute_b32 v221, v159, v220
	v_fma_f32 v218, v213, v216, v210
	s_waitcnt lgkmcnt(2)
	v_fma_f32 v218, v218, v214, v215
	v_fmac_f32_e32 v215, v216, v214
	v_fmac_f32_e32 v210, v213, v215
	v_cndmask_b32_e64 v214, v210, v218, s[0:1]
	v_fma_f32 v210, v211, v214, v220
	s_waitcnt lgkmcnt(0)
; #define LAS __attribute__((address_space(3)))
; template <bool FINAL, int z> __device__ __forceinline__ void rglru_blocks(LAS unsigned char* XCB, LAS float* XCF, LAS float* HS, const bf16x8 (&wa)[8], const bf16x8 (&wx)[8],
;         float ba, float bxx, float sp8, int r, int hh, int chl, float& st, float& CA, float& CB) {
;     ...
;         for (int bi = 0; bi < 2; ++bi) { const int tb = z ? 1 - bi : bi;
;             if (z == 1 && bi == 0) __builtin_amdgcn_s_sleep(8);
;             f32x16 ya, yx;
; #pragma unroll
;             for (int i = 0; i < 16; ++i) { ya[i] = ba; yx[i] = bxx; }
; #pragma unroll
;             for (int s = 0; s < 8; ++s) { const bf16x8 af = *(const LAS bf16x8*)(XCB + (32 * tb + r) * 272 + (16 * s + 8 * hh) * 2);
;                 ya = __builtin_amdgcn_mfma_f32_32x32x16_bf16(af, wa[s], ya, 0, 0, 0); yx = __builtin_amdgcn_mfma_f32_32x32x16_bf16(af, wx[s], yx, 0, 0, 0); }
;             float av[16], bv[16];
; #pragma unroll
;             for (int i = 0; i < 16; i += 2) {
;                 typedef float f2 __attribute__((ext_vector_type(2)));
;                 const f2 xc = {XCF[(32 * tb + crow(i, hh)) * 128 + chl], XCF[(32 * tb + crow(i + 1, hh)) * 128 + chl]};
;                 const f2 ta = (f2){ya[i], ya[i + 1]} * -1.4426950408889634f, tx = (f2){yx[i], yx[i + 1]} * -1.4426950408889634f;
;                 f2 ea, ex; ea.x = __builtin_amdgcn_exp2f(ta.x); ea.y = __builtin_amdgcn_exp2f(ta.y); ex.x = __builtin_amdgcn_exp2f(tx.x); ex.y = __builtin_amdgcn_exp2f(tx.y);
;                 const f2 da = ea + 1.0f, dx = ex + 1.0f;
;                 f2 rg, ig; rg.x = __builtin_amdgcn_rcpf(da.x); rg.y = __builtin_amdgcn_rcpf(da.y); ig.x = __builtin_amdgcn_rcpf(dx.x); ig.y = __builtin_amdgcn_rcpf(dx.y);
;                 const f2 la = rg * sp8; f2 a; a.x = __builtin_amdgcn_exp2f(la.x); a.y = __builtin_amdgcn_exp2f(la.y);
;                 const f2 om = a * -a + 1.0f; f2 sq; sq.x = __builtin_amdgcn_sqrtf(om.x); sq.y = __builtin_amdgcn_sqrtf(om.y);
;                 const f2 b = sq * ig * xc;
;     ...
;             if (FINAL) {
; #pragma unroll
;                 for (int g = 0; g < 4; ++g) { float hc = ent[g];
; #pragma unroll
;                     for (int k = 0; k < 4; ++k) { const int kk = z ? 3 - k : k; hc = av[4 * g + kk] * hc + bv[4 * g + kk];
;                         HS[(z * 64 + 32 * tb + 8 * g + 4 * hh + kk) * 128 + chl] = hc; } } }
	v_fma_f32 v210, v210, v212, v221
	v_fmac_f32_e32 v221, v214, v212
	v_cndmask_b32_e64 v212, v221, v218, s[0:1]
	v_fma_f32 v37, v37, v212, v55
	v_fmac_f32_e32 v54, v36, v37
	v_cndmask_b32_e64 v213, v215, v222, s[0:1]
	v_fma_f32 v35, v35, v54, v51
	v_fmac_f32_e32 v50, v34, v35
	v_fma_f32 v34, v41, v213, v57
	v_fmac_f32_e32 v56, v40, v34
	ds_write2st64_b32 v177, v56, v34 offset0:212 offset1:214
	v_fma_f32 v34, v39, v56, v53
	v_cndmask_b32_e64 v217, v225, v226, s[0:1]
	v_fmac_f32_e32 v52, v38, v34
	ds_write2st64_b32 v177, v52, v34 offset0:208 offset1:210
	v_fma_f32 v34, v61, v217, v45
	v_fmac_f32_e32 v44, v60, v34
	ds_write2st64_b32 v177, v44, v34 offset0:228 offset1:230
	v_fma_f32 v34, v43, v44, v59
	v_cndmask_b32_e64 v219, v223, v209, s[0:1]
	v_fmac_f32_e32 v58, v42, v34
	ds_write2st64_b32 v177, v58, v34 offset0:224 offset1:226
	v_fma_f32 v34, v65, v219, v49
	v_fmac_f32_e32 v48, v64, v34
	ds_write2st64_b32 v177, v48, v34 offset0:244 offset1:246
	v_fma_f32 v34, v63, v48, v47
	v_fmac_f32_e32 v46, v62, v34
	ds_write2st64_b32 v177, v54, v37 offset0:196 offset1:198
	ds_write2st64_b32 v177, v50, v35 offset0:192 offset1:194
	ds_write2st64_b32 v177, v46, v34 offset0:240 offset1:242
	ds_read_b128 v[212:215], v208
	ds_read_b128 v[216:219], v208 offset:32
	s_waitcnt lgkmcnt(1)
	v_mfma_f32_32x32x16_bf16 v[50:65], v[212:215], v[66:69], v[2:17]
	v_fmac_f32_e32 v220, v211, v221
	v_cndmask_b32_e64 v211, v220, v210, s[0:1]
	v_mfma_f32_32x32x16_bf16 v[34:49], v[212:215], v[98:101], v[18:33]
	s_waitcnt lgkmcnt(0)
	v_mfma_f32_32x32x16_bf16 v[50:65], v[216:219], v[70:73], v[50:65]
	v_mfma_f32_32x32x16_bf16 v[34:49], v[216:219], v[102:105], v[34:49]
	ds_read_b128 v[212:215], v208 offset:64
	ds_read_b128 v[216:219], v208 offset:96
	s_waitcnt lgkmcnt(1)
	v_mfma_f32_32x32x16_bf16 v[50:65], v[212:215], v[74:77], v[50:65]
	v_mfma_f32_32x32x16_bf16 v[34:49], v[212:215], v[106:109], v[34:49]
	s_waitcnt lgkmcnt(0)
	v_mfma_f32_32x32x16_bf16 v[50:65], v[216:219], v[78:81], v[50:65]
	v_mfma_f32_32x32x16_bf16 v[34:49], v[216:219], v[110:113], v[34:49]
	ds_read_b128 v[212:215], v208 offset:128
	ds_read_b128 v[216:219], v208 offset:160
	s_waitcnt lgkmcnt(1)
	v_mfma_f32_32x32x16_bf16 v[50:65], v[212:215], v[82:85], v[50:65]
	v_mfma_f32_32x32x16_bf16 v[34:49], v[212:215], v[114:117], v[34:49]
	s_waitcnt lgkmcnt(0)
	v_mfma_f32_32x32x16_bf16 v[50:65], v[216:219], v[86:89], v[50:65]
	v_mfma_f32_32x32x16_bf16 v[34:49], v[216:219], v[118:121], v[34:49]
	ds_read_b128 v[212:215], v208 offset:192
	ds_read_b128 v[216:219], v208 offset:224
	s_waitcnt lgkmcnt(1)
	v_mfma_f32_32x32x16_bf16 v[50:65], v[212:215], v[90:93], v[50:65]
	s_waitcnt lgkmcnt(0)
	v_mfma_f32_32x32x16_bf16 v[50:65], v[216:219], v[94:97], v[50:65]
	v_mfma_f32_32x32x16_bf16 v[34:49], v[212:215], v[122:125], v[34:49]
	s_nop 10
	v_mul_f32_e64 v50, v50, s12
	v_mul_f32_e64 v51, v51, s12
	v_mul_f32_e64 v54, v54, s12
	v_mul_f32_e64 v55, v55, s12
	v_exp_f32_e32 v50, v50
	v_exp_f32_e32 v51, v51
	v_pk_mul_f32 v[52:53], v[52:53], s[12:13] op_sel_hi:[1,0]
	v_exp_f32_e32 v54, v54
	v_exp_f32_e32 v55, v55
	v_mfma_f32_32x32x16_bf16 v[34:49], v[216:219], v[126:129], v[34:49]
	v_add_f32_e64 v50, v50, 1.0
	v_add_f32_e64 v51, v51, 1.0
	v_exp_f32_e32 v52, v52
	v_rcp_f32_e32 v50, v50
	v_rcp_f32_e32 v51, v51
	v_exp_f32_e32 v53, v53
	v_pk_add_f32 v[54:55], v[54:55], 1.0 op_sel_hi:[1,0]
	ds_read2st64_b32 v[212:213], v175 offset0:68 offset1:70
	s_nop 3
	v_pk_mul_f32 v[34:35], v[34:35], s[12:13] op_sel_hi:[1,0]
	v_pk_add_f32 v[52:53], v[52:53], 1.0 op_sel_hi:[1,0]
	v_exp_f32_e32 v214, v34
	v_exp_f32_e32 v215, v35
	v_pk_mul_f32 v[34:35], v[182:183], v[50:51]
	v_rcp_f32_e32 v54, v54
	v_exp_f32_e32 v34, v34
	v_exp_f32_e32 v35, v35
	v_pk_add_f32 v[50:51], v[214:215], 1.0 op_sel_hi:[1,0]
	v_rcp_f32_e32 v55, v55
	v_rcp_f32_e32 v50, v50
	v_pk_fma_f32 v[214:215], v[34:35], v[34:35], 1.0 op_sel_hi:[1,1,0] neg_lo:[1,0,0] neg_hi:[1,0,0]
	v_rcp_f32_e32 v51, v51
	v_sqrt_f32_e32 v214, v214
	v_sqrt_f32_e32 v215, v215
	v_rcp_f32_e32 v52, v52
	v_rcp_f32_e32 v53, v53
	v_pk_mul_f32 v[38:39], v[38:39], s[12:13] op_sel_hi:[1,0]
	v_pk_mul_f32 v[50:51], v[50:51], v[214:215]
	v_pk_mul_f32 v[36:37], v[36:37], s[12:13] op_sel_hi:[1,0]
	v_exp_f32_e32 v216, v38
	v_exp_f32_e32 v217, v39
	v_pk_mul_f32 v[38:39], v[182:183], v[54:55]
	s_waitcnt lgkmcnt(0)
	v_pk_mul_f32 v[50:51], v[212:213], v[50:51]
	v_exp_f32_e32 v212, v36
	v_exp_f32_e32 v213, v37
	v_pk_mul_f32 v[36:37], v[182:183], v[52:53]
	v_exp_f32_e32 v38, v38
	v_exp_f32_e32 v39, v39
	v_exp_f32_e32 v36, v36
	v_exp_f32_e32 v37, v37
	v_pk_add_f32 v[54:55], v[216:217], 1.0 op_sel_hi:[1,0]
	v_pk_add_f32 v[52:53], v[212:213], 1.0 op_sel_hi:[1,0]
	v_rcp_f32_e32 v216, v54
	v_rcp_f32_e32 v217, v55
	v_pk_fma_f32 v[54:55], v[38:39], v[38:39], 1.0 op_sel_hi:[1,1,0] neg_lo:[1,0,0] neg_hi:[1,0,0]
	v_pk_fma_f32 v[212:213], v[36:37], v[36:37], 1.0 op_sel_hi:[1,1,0] neg_lo:[1,0,0] neg_hi:[1,0,0]
	v_sqrt_f32_e32 v218, v54
	v_sqrt_f32_e32 v219, v55
	v_pk_mul_f32 v[54:55], v[56:57], s[12:13] op_sel_hi:[1,0]
	v_rcp_f32_e32 v52, v52
	v_rcp_f32_e32 v53, v53
	v_sqrt_f32_e32 v212, v212
	v_sqrt_f32_e32 v213, v213
	v_exp_f32_e32 v56, v54
	v_exp_f32_e32 v57, v55
	ds_read2st64_b32 v[214:215], v175 offset0:72 offset1:74
	v_pk_mul_f32 v[58:59], v[58:59], s[12:13] op_sel_hi:[1,0]
	v_pk_mul_f32 v[52:53], v[52:53], v[212:213]
	ds_read2st64_b32 v[212:213], v175 offset0:84 offset1:86
	v_pk_add_f32 v[56:57], v[56:57], 1.0 op_sel_hi:[1,0]
	v_exp_f32_e32 v58, v58
	v_exp_f32_e32 v59, v59
	v_rcp_f32_e32 v56, v56
	v_rcp_f32_e32 v57, v57
	s_waitcnt lgkmcnt(1)
; template <bool FINAL, int z> __device__ __forceinline__ void rglru_blocks(LAS unsigned char* XCB, LAS float* XCF, LAS float* HS, const bf16x8 (&wa)[8], const bf16x8 (&wx)[8],
;         float ba, float bxx, float sp8, int r, int hh, int chl, float& st, float& CA, float& CB) {
;     ...
;                 const f2 ta = (f2){ya[i], ya[i + 1]} * -1.4426950408889634f, tx = (f2){yx[i], yx[i + 1]} * -1.4426950408889634f;
;                 f2 ea, ex; ea.x = __builtin_amdgcn_exp2f(ta.x); ea.y = __builtin_amdgcn_exp2f(ta.y); ex.x = __builtin_amdgcn_exp2f(tx.x); ex.y = __builtin_amdgcn_exp2f(tx.y);
;                 const f2 da = ea + 1.0f, dx = ex + 1.0f;
;                 f2 rg, ig; rg.x = __builtin_amdgcn_rcpf(da.x); rg.y = __builtin_amdgcn_rcpf(da.y); ig.x = __builtin_amdgcn_rcpf(dx.x); ig.y = __builtin_amdgcn_rcpf(dx.y);
;                 const f2 la = rg * sp8; f2 a; a.x = __builtin_amdgcn_exp2f(la.x); a.y = __builtin_amdgcn_exp2f(la.y);
;                 const f2 om = a * -a + 1.0f; f2 sq; sq.x = __builtin_amdgcn_sqrtf(om.x); sq.y = __builtin_amdgcn_sqrtf(om.y);
;                 const f2 b = sq * ig * xc;
;                 av[i] = a.x; av[i + 1] = a.y; bv[i] = b.x; bv[i + 1] = b.y; }
;             float Ag[4], Bg[4], Ap[4], Bp[4];
; #pragma unroll
;             for (int g = 0; g < 4; ++g) { float A = 1.f, B = 0.f;
; #pragma unroll
;                 for (int k = 0; k < 4; ++k) { const int kk = z ? 3 - k : k; B = B * av[4 * g + kk] + bv[4 * g + kk]; A *= av[4 * g + kk]; }
;                 Ag[g] = A; Bg[g] = B; Ap[g] = __shfl_xor(A, 32); Bp[g] = __shfl_xor(B, 32); }
;             float ent[4]; float cur = st;
; #pragma unroll
;             for (int gi = 0; gi < 4; ++gi) { const int g = z ? 3 - gi : gi;
;                 const bool own_first = z ? (hh == 1) : (hh == 0);
;                 if (own_first) { ent[g] = cur; cur = Ag[g] * cur + Bg[g]; CB = Ag[g] * CB + Bg[g]; CA *= Ag[g]; cur = Ap[g] * cur + Bp[g]; CB = Ap[g] * CB + Bp[g]; CA *= Ap[g]; }
;                 else { cur = Ap[g] * cur + Bp[g]; CB = Ap[g] * CB + Bp[g]; CA *= Ap[g]; ent[g] = cur; cur = Ag[g] * cur + Bg[g]; CB = Ag[g] * CB + Bg[g]; CA *= Ag[g]; } }
;             st = cur;
;             if (FINAL) {
; #pragma unroll
;                 for (int g = 0; g < 4; ++g) { float hc = ent[g];
; #pragma unroll
	v_pk_mul_f32 v[54:55], v[214:215], v[52:53]
	v_pk_mul_f32 v[52:53], v[216:217], v[218:219]
	v_pk_mul_f32 v[40:41], v[40:41], s[12:13] op_sel_hi:[1,0]
	v_pk_add_f32 v[58:59], v[58:59], 1.0 op_sel_hi:[1,0]
	s_waitcnt lgkmcnt(0)
	v_pk_mul_f32 v[52:53], v[212:213], v[52:53]
	v_exp_f32_e32 v212, v40
	v_exp_f32_e32 v213, v41
	v_pk_mul_f32 v[40:41], v[182:183], v[56:57]
	v_rcp_f32_e32 v58, v58
	v_rcp_f32_e32 v59, v59
	v_pk_mul_f32 v[60:61], v[60:61], s[12:13] op_sel_hi:[1,0]
	v_exp_f32_e32 v40, v40
	v_exp_f32_e32 v41, v41
	v_exp_f32_e32 v60, v60
	v_exp_f32_e32 v61, v61
	v_pk_mul_f32 v[64:65], v[64:65], s[12:13] op_sel_hi:[1,0]
	v_pk_mul_f32 v[42:43], v[42:43], s[12:13] op_sel_hi:[1,0]
	v_exp_f32_e32 v64, v64
	v_exp_f32_e32 v65, v65
	v_exp_f32_e32 v216, v42
	v_exp_f32_e32 v217, v43
	v_pk_mul_f32 v[42:43], v[182:183], v[58:59]
	v_pk_mul_f32 v[62:63], v[62:63], s[12:13] op_sel_hi:[1,0]
	v_pk_add_f32 v[56:57], v[212:213], 1.0 op_sel_hi:[1,0]
	v_pk_fma_f32 v[212:213], v[40:41], v[40:41], 1.0 op_sel_hi:[1,1,0] neg_lo:[1,0,0] neg_hi:[1,0,0]
	v_exp_f32_e32 v42, v42
	v_exp_f32_e32 v43, v43
	v_pk_add_f32 v[60:61], v[60:61], 1.0 op_sel_hi:[1,0]
	v_exp_f32_e32 v62, v62
	v_exp_f32_e32 v63, v63
	v_rcp_f32_e32 v56, v56
	v_rcp_f32_e32 v57, v57
	v_sqrt_f32_e32 v212, v212
	v_sqrt_f32_e32 v213, v213
	v_rcp_f32_e32 v60, v60
	v_rcp_f32_e32 v61, v61
	v_pk_add_f32 v[64:65], v[64:65], 1.0 op_sel_hi:[1,0]
	v_pk_add_f32 v[58:59], v[216:217], 1.0 op_sel_hi:[1,0]
	v_rcp_f32_e32 v64, v64
	v_rcp_f32_e32 v65, v65
	v_pk_fma_f32 v[216:217], v[42:43], v[42:43], 1.0 op_sel_hi:[1,1,0] neg_lo:[1,0,0] neg_hi:[1,0,0]
	v_pk_add_f32 v[62:63], v[62:63], 1.0 op_sel_hi:[1,0]
	v_pk_mul_f32 v[56:57], v[56:57], v[212:213]
	ds_read2st64_b32 v[212:213], v175 offset0:100 offset1:102
	v_rcp_f32_e32 v58, v58
	v_rcp_f32_e32 v59, v59
	v_sqrt_f32_e32 v216, v216
	v_sqrt_f32_e32 v217, v217
	v_pk_mul_f32 v[44:45], v[44:45], s[12:13] op_sel_hi:[1,0]
	v_pk_mul_f32 v[60:61], v[182:183], v[60:61]
	v_rcp_f32_e32 v62, v62
	v_rcp_f32_e32 v63, v63
	v_exp_f32_e32 v44, v44
	v_exp_f32_e32 v45, v45
	v_exp_f32_e32 v60, v60
	v_exp_f32_e32 v61, v61
	v_pk_mul_f32 v[48:49], v[48:49], s[12:13] op_sel_hi:[1,0]
	v_pk_mul_f32 v[64:65], v[182:183], v[64:65]
	v_exp_f32_e32 v48, v48
	v_exp_f32_e32 v49, v49
	v_exp_f32_e32 v64, v64
	v_exp_f32_e32 v65, v65
	v_pk_mul_f32 v[58:59], v[58:59], v[216:217]
	v_pk_mul_f32 v[46:47], v[46:47], s[12:13] op_sel_hi:[1,0]
	v_pk_mul_f32 v[62:63], v[182:183], v[62:63]
	s_waitcnt lgkmcnt(0)
	v_pk_mul_f32 v[58:59], v[212:213], v[58:59]
	v_pk_add_f32 v[44:45], v[44:45], 1.0 op_sel_hi:[1,0]
	v_pk_fma_f32 v[212:213], v[60:61], v[60:61], 1.0 op_sel_hi:[1,1,0] neg_lo:[1,0,0] neg_hi:[1,0,0]
	v_exp_f32_e32 v46, v46
	v_exp_f32_e32 v47, v47
	v_exp_f32_e32 v62, v62
	v_exp_f32_e32 v63, v63
	v_rcp_f32_e32 v44, v44
	v_rcp_f32_e32 v45, v45
	v_sqrt_f32_e32 v212, v212
	v_sqrt_f32_e32 v213, v213
	ds_read2st64_b32 v[214:215], v175 offset0:88 offset1:90
	v_pk_add_f32 v[48:49], v[48:49], 1.0 op_sel_hi:[1,0]
	v_pk_fma_f32 v[220:221], v[64:65], v[64:65], 1.0 op_sel_hi:[1,1,0] neg_lo:[1,0,0] neg_hi:[1,0,0]
	ds_read2st64_b32 v[218:219], v175 offset0:120 offset1:122
	v_rcp_f32_e32 v48, v48
	v_rcp_f32_e32 v49, v49
	v_sqrt_f32_e32 v220, v220
	v_sqrt_f32_e32 v221, v221
	v_pk_add_f32 v[46:47], v[46:47], 1.0 op_sel_hi:[1,0]
	v_pk_fma_f32 v[216:217], v[62:63], v[62:63], 1.0 op_sel_hi:[1,1,0] neg_lo:[1,0,0] neg_hi:[1,0,0]
	v_pk_mul_f32 v[44:45], v[44:45], v[212:213]
	ds_read2st64_b32 v[212:213], v175 offset0:116 offset1:118
	v_rcp_f32_e32 v46, v46
	v_rcp_f32_e32 v47, v47
	v_sqrt_f32_e32 v216, v216
	v_sqrt_f32_e32 v217, v217
	s_waitcnt lgkmcnt(2)
	v_pk_mul_f32 v[56:57], v[214:215], v[56:57]
	ds_read2st64_b32 v[214:215], v175 offset0:104 offset1:106
	v_pk_mul_f32 v[48:49], v[48:49], v[220:221]
	v_pk_mul_f32 v[46:47], v[46:47], v[216:217]
	s_waitcnt lgkmcnt(2)
	v_pk_mul_f32 v[48:49], v[218:219], v[48:49]
	s_waitcnt lgkmcnt(1)
	v_pk_mul_f32 v[46:47], v[212:213], v[46:47]
	v_fma_f32 v220, 0, v65, v49
	v_fma_f32 v220, v64, v220, v48
	v_mul_f32_e32 v221, v65, v64
	v_fma_f32 v220, v63, v220, v47
	v_mul_f32_e32 v221, v63, v221
	s_waitcnt lgkmcnt(0)
	v_pk_mul_f32 v[44:45], v[214:215], v[44:45]
	v_fma_f32 v220, v62, v220, v46
	v_mul_f32_e32 v221, v62, v221
	v_fma_f32 v218, 0, v61, v45
	ds_bpermute_b32 v222, v159, v221
	ds_bpermute_b32 v223, v159, v220
	v_fma_f32 v218, v60, v218, v44
	v_mul_f32_e32 v219, v61, v60
	v_fma_f32 v218, v43, v218, v59
	v_mul_f32_e32 v219, v43, v219
	v_fma_f32 v218, v42, v218, v58
	v_mul_f32_e32 v219, v42, v219
	v_fma_f32 v214, 0, v41, v57
	ds_bpermute_b32 v224, v159, v219
	ds_bpermute_b32 v225, v159, v218
	v_fma_f32 v226, v211, v221, v220
	v_fma_f32 v214, v40, v214, v56
	v_mul_f32_e32 v215, v41, v40
	s_waitcnt lgkmcnt(2)
	v_fma_f32 v226, v226, v222, v223
	v_fmac_f32_e32 v223, v211, v222
	v_fma_f32 v214, v39, v214, v53
	v_mul_f32_e32 v215, v39, v215
	v_fmac_f32_e32 v220, v221, v223
	v_fma_f32 v212, 0, v37, v55
	v_fma_f32 v214, v38, v214, v52
	v_mul_f32_e32 v215, v38, v215
	v_cndmask_b32_e64 v211, v220, v226, s[0:1]
	v_fma_f32 v212, v36, v212, v54
	v_mul_f32_e32 v213, v37, v36
	ds_bpermute_b32 v216, v159, v215
	ds_bpermute_b32 v217, v159, v214
	v_fma_f32 v220, v219, v211, v218
	v_fma_f32 v212, v35, v212, v51
	v_mul_f32_e32 v213, v35, v213
	s_waitcnt lgkmcnt(2)
	v_fma_f32 v220, v220, v224, v225
	v_fmac_f32_e32 v225, v211, v224
	v_fma_f32 v212, v34, v212, v50
	v_mul_f32_e32 v213, v34, v213
	v_fmac_f32_e32 v218, v219, v225
	ds_bpermute_b32 v213, v159, v213
	ds_bpermute_b32 v212, v159, v212
	v_cndmask_b32_e64 v218, v218, v220, s[0:1]
	v_fma_f32 v219, v215, v218, v214
	s_waitcnt lgkmcnt(2)
	v_fma_f32 v219, v219, v216, v217
	v_fmac_f32_e32 v217, v218, v216
	v_fmac_f32_e32 v214, v215, v217
	v_cndmask_b32_e64 v214, v214, v219, s[0:1]
	s_waitcnt lgkmcnt(0)
	v_fmac_f32_e32 v212, v214, v213
	v_cndmask_b32_e64 v212, v212, v219, s[0:1]
	v_fma_f32 v37, v37, v212, v55
	v_fmac_f32_e32 v54, v36, v37
	v_cndmask_b32_e64 v215, v217, v220, s[0:1]
	v_fma_f32 v35, v35, v54, v51
	v_fmac_f32_e32 v50, v34, v35
	v_fma_f32 v34, v41, v215, v57
	v_fmac_f32_e32 v56, v40, v34
	ds_write2st64_b32 v177, v56, v34 offset0:148 offset1:150
	v_fma_f32 v34, v39, v56, v53
	v_cndmask_b32_e64 v211, v225, v226, s[0:1]
	v_fmac_f32_e32 v52, v38, v34
	ds_write2st64_b32 v177, v52, v34 offset0:144 offset1:146
	v_fma_f32 v34, v61, v211, v45
	v_fmac_f32_e32 v44, v60, v34
	ds_write2st64_b32 v177, v44, v34 offset0:164 offset1:166
	v_fma_f32 v34, v43, v44, v59
	v_cndmask_b32_e64 v210, v223, v210, s[0:1]
	v_fmac_f32_e32 v58, v42, v34
	ds_write2st64_b32 v177, v58, v34 offset0:160 offset1:162
	v_fma_f32 v34, v65, v210, v49
	v_fmac_f32_e32 v48, v64, v34
	ds_write2st64_b32 v177, v48, v34 offset0:180 offset1:182
	v_fma_f32 v34, v63, v48, v47
	v_fmac_f32_e32 v46, v62, v34
	ds_write2st64_b32 v177, v54, v37 offset0:132 offset1:134
	ds_write2st64_b32 v177, v50, v35 offset0:128 offset1:130
	ds_write2st64_b32 v177, v46, v34 offset0:176 offset1:178
